# P6: the per-group vmcnt(0) drain (left over from the hoisted router-bias load) moved from before the router top-k to the loop-back block where the prefetched rows are first read
# baseline (speedup 1.0000x reference)
.LBB0_981:
	s_waitcnt vmcnt(0)
	v_readlane_b32 s12, v252, 57
	v_mov_b64_e32 v[192:193], v[104:105]
	v_mov_b64_e32 v[188:189], v[108:109]
	v_mov_b64_e32 v[184:185], v[112:113]
	v_mov_b64_e32 v[180:181], v[116:117]
	v_mov_b64_e32 v[176:177], v[124:125]
	v_mov_b64_e32 v[172:173], v[128:129]
	v_mov_b64_e32 v[168:169], v[132:133]
	v_mov_b64_e32 v[164:165], v[136:137]
	v_add_u32_e32 v208, s71, v208
	s_add_i32 s14, s14, s12
	s_and_b64 vcc, exec, s[30:31]
	v_mov_b64_e32 v[190:191], v[102:103]
	v_mov_b64_e32 v[186:187], v[106:107]
	v_mov_b64_e32 v[182:183], v[110:111]
	v_mov_b64_e32 v[178:179], v[114:115]
	v_mov_b64_e32 v[174:175], v[122:123]
	v_mov_b64_e32 v[170:171], v[126:127]
	v_mov_b64_e32 v[166:167], v[130:131]
	v_mov_b64_e32 v[162:163], v[134:135]
	s_mov_b32 s12, s49
	s_cbranch_vccnz .LBB0_1030

.LBB0_986:
	v_mov_b32_e32 v246, v191
	v_mov_b32_e32 v247, v192
	v_mov_b32_e32 v248, v190
	v_mov_b32_e32 v249, v193
	v_pk_add_f32 v[246:247], v[246:247], v[248:249]
	v_mov_b32_e32 v248, v187
	v_mov_b32_e32 v249, v188
	v_mov_b32_e32 v216, v186
	v_mov_b32_e32 v217, v189
	v_pk_add_f32 v[216:217], v[248:249], v[216:217]
	v_add_f32_e32 v209, v246, v247
	v_pk_add_f32 v[216:217], v[216:217], v[216:217] op_sel:[0,1] op_sel_hi:[1,0]
	v_add_f32_e32 v246, 0, v209
	v_add_f32_e32 v248, v182, v183
	v_add_f32_e32 v218, v184, v185
	v_mov_b32_e32 v247, v178
	v_mov_b32_e32 v217, v179
	v_mov_b32_e32 v249, v180
	v_mov_b32_e32 v219, v181
	v_pk_add_f32 v[216:217], v[246:247], v[216:217]
	v_pk_add_f32 v[218:219], v[248:249], v[218:219]
	s_mov_b32 s36, 0xf800000
	v_pk_add_f32 v[216:217], v[216:217], v[218:219]
	s_nop 0
	v_add_f32_e32 v209, v216, v217
	ds_bpermute_b32 v216, v226, v209
	s_waitcnt lgkmcnt(0)
	v_add_f32_e32 v209, v209, v216
	ds_bpermute_b32 v216, v227, v209
	s_waitcnt lgkmcnt(0)
	v_add_f32_e32 v209, v209, v216
	ds_bpermute_b32 v216, v228, v209
	s_waitcnt lgkmcnt(0)
	v_add_f32_e32 v209, v209, v216
	ds_bpermute_b32 v216, v229, v209
	s_waitcnt lgkmcnt(0)
	v_add_f32_e32 v209, v209, v216
	ds_bpermute_b32 v216, v230, v209
	s_waitcnt lgkmcnt(0)
	v_add_f32_e32 v209, v209, v216
	ds_bpermute_b32 v216, v231, v209
	s_waitcnt lgkmcnt(0)
	v_add_f32_e32 v209, v209, v216
	v_fmamk_f32 v191, v209, 0xba800000, v191
	v_fmamk_f32 v190, v209, 0xba800000, v190
	v_fmamk_f32 v193, v209, 0xba800000, v193
	v_fmac_f32_e32 v192, 0xba800000, v209
	v_pk_mul_f32 v[216:217], v[192:193], v[192:193]
	v_pk_mul_f32 v[218:219], v[190:191], v[190:191]
	v_fmamk_f32 v187, v209, 0xba800000, v187
	v_fmamk_f32 v186, v209, 0xba800000, v186
	v_fmamk_f32 v189, v209, 0xba800000, v189
	v_pk_mov_b32 v[246:247], v[218:219], v[216:217] op_sel:[1,0]
	v_mov_b32_e32 v219, v217
	v_fmac_f32_e32 v188, 0xba800000, v209
	v_pk_add_f32 v[216:217], v[246:247], v[218:219]
	v_pk_mul_f32 v[218:219], v[188:189], v[188:189]
	v_pk_mul_f32 v[246:247], v[186:187], v[186:187]
	v_fmac_f32_e32 v184, 0xba800000, v209
	v_pk_mov_b32 v[248:249], v[246:247], v[218:219] op_sel:[1,0]
	v_mov_b32_e32 v247, v219
	v_pk_add_f32 v[218:219], v[248:249], v[246:247]
	v_fmamk_f32 v246, v209, 0xba800000, v182
	v_fmamk_f32 v247, v209, 0xba800000, v183
	v_mul_f32_e32 v182, v246, v246
	v_pk_fma_f32 v[182:183], v[246:247], v[246:247], v[182:183] op_sel_hi:[1,1,0]
	v_fmamk_f32 v185, v209, 0xba800000, v185
	v_mul_f32_e32 v182, v184, v184
	v_pk_add_f32 v[216:217], v[216:217], v[216:217] op_sel_hi:[0,1]
	v_pk_add_f32 v[218:219], v[218:219], v[218:219] op_sel_hi:[0,1]
	v_pk_fma_f32 v[248:249], v[184:185], v[184:185], v[182:183] op_sel_hi:[1,1,0]
	v_fmamk_f32 v181, v209, 0xba800000, v181
	v_fmamk_f32 v180, v209, 0xba800000, v180
	v_fmamk_f32 v179, v209, 0xba800000, v179
	v_fmac_f32_e32 v178, 0xba800000, v209
	v_mul_f32_e32 v182, v178, v178
	v_mul_f32_e32 v248, v179, v179
	v_mul_f32_e32 v216, v180, v180
	v_mul_f32_e32 v218, v181, v181
	v_pk_add_f32 v[182:183], v[182:183], v[248:249]
	v_pk_add_f32 v[216:217], v[216:217], v[218:219]
	s_nop 0
	v_pk_add_f32 v[182:183], v[182:183], v[216:217]
	s_nop 0
	v_add_f32_e32 v182, v182, v183
	ds_bpermute_b32 v183, v226, v182
	s_waitcnt lgkmcnt(0)
	v_add_f32_e32 v182, v182, v183
	ds_bpermute_b32 v183, v227, v182
	s_waitcnt lgkmcnt(0)
	v_add_f32_e32 v182, v182, v183
	ds_bpermute_b32 v183, v228, v182
	s_waitcnt lgkmcnt(0)
	v_add_f32_e32 v182, v182, v183
	ds_bpermute_b32 v183, v229, v182
	s_waitcnt lgkmcnt(0)
	v_add_f32_e32 v182, v182, v183
	ds_bpermute_b32 v183, v230, v182
	s_waitcnt lgkmcnt(0)
	v_add_f32_e32 v182, v182, v183
	ds_bpermute_b32 v183, v231, v182
	s_waitcnt lgkmcnt(0)
	v_add_f32_e32 v182, v182, v183
	v_fmamk_f32 v182, v182, 0x3a800000, v211
	v_mul_f32_e32 v183, 0x4f800000, v182
	v_cmp_gt_f32_e32 vcc, s36, v182
	s_nop 1
	v_cndmask_b32_e32 v182, v182, v183, vcc
	v_sqrt_f32_e32 v183, v182
	s_nop 0
	v_add_u32_e32 v209, -1, v183
	v_add_u32_e32 v216, 1, v183
	v_fma_f32 v217, -v209, v183, v182
	v_fma_f32 v218, -v216, v183, v182
	v_cmp_ge_f32_e64 s[12:13], 0, v217
	s_nop 1
	v_cndmask_b32_e64 v183, v183, v209, s[12:13]
	v_cmp_lt_f32_e64 s[12:13], 0, v218
	s_nop 1
	v_cndmask_b32_e64 v183, v183, v216, s[12:13]
	v_mul_f32_e32 v209, 0x37800000, v183
	v_cndmask_b32_e32 v183, v183, v209, vcc
	v_cmp_class_f32_e32 vcc, v182, v212
	s_nop 1
	v_cndmask_b32_e32 v182, v183, v182, vcc
	v_div_scale_f32 v183, s[12:13], v182, v182, 1.0
	v_rcp_f32_e32 v209, v183
	v_readlane_b32 s12, v252, 4
	s_add_i32 s34, s12, s14
	s_ashr_i32 s35, s34, 31
	v_fma_f32 v216, -v183, v209, 1.0
	v_fmac_f32_e32 v209, v216, v209
	v_div_scale_f32 v216, vcc, 1.0, v182, 1.0
	v_mul_f32_e32 v217, v216, v209
	v_fma_f32 v218, -v183, v217, v216
	v_fmac_f32_e32 v217, v218, v209
	v_fma_f32 v183, -v183, v217, v216
	v_div_fmas_f32 v183, v183, v209, v217
	v_div_fixup_f32 v182, v183, v182, 1.0
	v_pk_mul_f32 v[190:191], v[190:191], v[182:183] op_sel_hi:[1,0]
	s_lshl_b64 s[12:13], s[34:35], 10
	s_waitcnt vmcnt(22)
	v_pk_fma_f32 v[190:191], v[2:3], v[190:191], v[6:7]
	v_pk_mul_f32 v[192:193], v[192:193], v[182:183] op_sel_hi:[1,0]
	v_pk_fma_f32 v[190:191], v[98:99], v[190:191], v[118:119]
	s_mov_b32 s35, 0xffff
	v_cvt_pk_bf16_f32 v216, v191, 0
	v_cvt_pk_bf16_f32 v183, v190, 0
	v_lshlrev_b32_e32 v216, 16, v216
	v_lshlrev_b32_e32 v209, 16, v183
	v_sub_f32_e32 v217, v191, v216
	v_and_or_b32 v216, v183, s35, v216
	v_mov_b32_e32 v183, v1
	v_cvt_pk_fp8_f32 v183, v190, v191
	v_pk_fma_f32 v[192:193], v[4:5], v[192:193], v[8:9]
	v_cvt_pk_bf16_f32 v218, v217, 0
	v_pk_fma_f32 v[192:193], v[100:101], v[192:193], v[120:121]
	v_sub_f32_e32 v209, v190, v209
	v_cvt_pk_fp8_f32 v183, v192, v193 op_sel:[0,0,1]
	v_cvt_pk_bf16_f32 v217, v192, 0
	v_cvt_pk_bf16_f32 v248, v193, 0
	v_lshlrev_b32_e32 v219, 16, v217
	v_lshlrev_b32_e32 v248, 16, v248
	v_sub_f32_e32 v219, v192, v219
	v_sub_f32_e32 v249, v193, v248
	v_lshl_add_u64 v[192:193], v[202:203], 0, s[12:13]
	global_store_dword v[192:193], v183, off
	v_add_u32_e32 v183, s47, v234
	v_pk_mul_f32 v[186:187], v[186:187], v[182:183] op_sel_hi:[1,0]
	v_cvt_pk_bf16_f32 v249, v249, 0
	s_waitcnt vmcnt(20)
	v_pk_fma_f32 v[186:187], v[10:11], v[186:187], v[18:19]
	v_cvt_pk_bf16_f32 v209, v209, 0
	v_cvt_pk_bf16_f32 v219, v219, 0
	v_and_or_b32 v217, v217, s35, v248
	v_lshlrev_b32_e32 v190, 16, v218
	v_lshlrev_b32_e32 v191, 16, v249
	v_pk_fma_f32 v[186:187], v[138:139], v[186:187], v[142:143]
	v_and_or_b32 v190, v209, s35, v190
	v_and_or_b32 v191, v219, s35, v191
	ds_write_b64 v183, v[216:217]
	ds_write_b64 v183, v[190:191] offset:33024
	v_pk_mul_f32 v[188:189], v[188:189], v[182:183] op_sel_hi:[1,0]
	v_cvt_pk_bf16_f32 v183, v186, 0
	v_lshlrev_b32_e32 v190, 16, v183
	v_sub_f32_e32 v190, v186, v190
	v_cvt_pk_bf16_f32 v192, v190, 0
	v_cvt_pk_bf16_f32 v190, v187, 0
	v_lshlrev_b32_e32 v190, 16, v190
	v_sub_f32_e32 v191, v187, v190
	v_cvt_pk_bf16_f32 v193, v191, 0
	v_and_or_b32 v190, v183, s35, v190
	v_lshlrev_b32_e32 v183, 16, v193
	v_mov_b32_e32 v193, v1
	v_pk_fma_f32 v[188:189], v[12:13], v[188:189], v[20:21]
	v_cvt_pk_fp8_f32 v193, v186, v187
	v_pk_fma_f32 v[188:189], v[140:141], v[188:189], v[144:145]
	s_add_u32 s12, s20, s12
	v_cvt_pk_bf16_f32 v216, v189, 0
	v_cvt_pk_bf16_f32 v191, v188, 0
	v_lshlrev_b32_e32 v216, 16, v216
	v_lshlrev_b32_e32 v209, 16, v191
	v_sub_f32_e32 v217, v189, v216
	v_cvt_pk_fp8_f32 v193, v188, v189 op_sel:[0,0,1]
	v_sub_f32_e32 v209, v188, v209
	v_cvt_pk_bf16_f32 v217, v217, 0
	v_cvt_pk_bf16_f32 v209, v209, 0
	v_and_or_b32 v186, v192, s35, v183
	v_lshlrev_b32_e32 v183, 16, v217
	s_addc_u32 s13, s21, s13
	v_and_or_b32 v191, v191, s35, v216
	v_and_or_b32 v187, v209, s35, v183
	v_lshl_add_u64 v[188:189], s[12:13], 0, v[0:1]
	v_add_u32_e32 v183, s47, v235
	global_store_dword v[188:189], v193, off
	ds_write_b64 v183, v[190:191]
	ds_write_b64 v183, v[186:187] offset:33024
	v_pk_mul_f32 v[186:187], v[246:247], v[182:183] op_sel_hi:[1,0]
	v_pk_mul_f32 v[184:185], v[184:185], v[182:183] op_sel_hi:[1,0]
	s_waitcnt vmcnt(20)
	v_pk_fma_f32 v[186:187], v[14:15], v[186:187], v[22:23]
	v_pk_fma_f32 v[184:185], v[16:17], v[184:185], v[24:25]
	v_pk_fma_f32 v[186:187], v[150:151], v[186:187], v[146:147]
	v_pk_fma_f32 v[184:185], v[152:153], v[184:185], v[148:149]
	v_cvt_pk_bf16_f32 v183, v186, 0
	v_lshlrev_b32_e32 v188, 16, v183
	v_sub_f32_e32 v188, v186, v188
	v_cvt_pk_bf16_f32 v209, v188, 0
	v_cvt_pk_bf16_f32 v188, v187, 0
	v_lshlrev_b32_e32 v218, 16, v188
	v_sub_f32_e32 v188, v187, v218
	v_cvt_pk_bf16_f32 v246, v184, 0
	v_cvt_pk_bf16_f32 v219, v188, 0
	v_lshlrev_b32_e32 v188, 16, v246
	v_sub_f32_e32 v188, v184, v188
	v_cvt_pk_bf16_f32 v247, v188, 0
	v_mov_b32_e32 v188, v175
	v_mov_b32_e32 v189, v176
	v_mov_b32_e32 v190, v174
	v_mov_b32_e32 v191, v177
	v_pk_add_f32 v[188:189], v[188:189], v[190:191]
	v_mov_b32_e32 v190, v171
	v_mov_b32_e32 v191, v172
	v_mov_b32_e32 v192, v170
	v_mov_b32_e32 v193, v173
	v_pk_add_f32 v[190:191], v[190:191], v[192:193]
	v_add_f32_e32 v188, v188, v189
	v_pk_add_f32 v[190:191], v[190:191], v[190:191] op_sel:[0,1] op_sel_hi:[1,0]
	v_add_f32_e32 v188, 0, v188
	v_add_f32_e32 v192, v166, v167
	v_add_f32_e32 v216, v168, v169
	v_mov_b32_e32 v189, v162
	v_mov_b32_e32 v191, v163
	v_mov_b32_e32 v193, v164
	v_mov_b32_e32 v217, v165
	v_pk_add_f32 v[188:189], v[188:189], v[190:191]
	v_pk_add_f32 v[190:191], v[192:193], v[216:217]
	v_cvt_pk_bf16_f32 v248, v185, 0
	v_pk_add_f32 v[188:189], v[188:189], v[190:191]
	v_lshlrev_b32_e32 v191, 16, v248
	v_add_f32_e32 v189, v188, v189
	ds_bpermute_b32 v190, v226, v189
	v_sub_f32_e32 v188, v185, v191
	v_cvt_pk_bf16_f32 v192, v188, 0
	v_and_or_b32 v188, v183, s35, v218
	v_mov_b32_e32 v193, v1
	s_waitcnt lgkmcnt(0)
	v_add_f32_e32 v183, v189, v190
	ds_bpermute_b32 v190, v227, v183
	v_cvt_pk_fp8_f32 v193, v186, v187
	v_and_or_b32 v189, v246, s35, v191
	v_lshlrev_b32_e32 v191, 16, v219
	v_and_or_b32 v186, v209, s35, v191
	s_waitcnt lgkmcnt(0)
	v_add_f32_e32 v183, v183, v190
	ds_bpermute_b32 v190, v228, v183
	v_cvt_pk_fp8_f32 v193, v184, v185 op_sel:[0,0,1]
	v_lshl_add_u64 v[184:185], s[12:13], 0, v[198:199]
	v_lshlrev_b32_e32 v187, 16, v192
	v_and_or_b32 v187, v247, s35, v187
	s_waitcnt lgkmcnt(0)
	v_add_f32_e32 v183, v183, v190
	ds_bpermute_b32 v190, v229, v183
	global_store_dword v[184:185], v193, off
	v_add_u32_e32 v184, s47, v236
	ds_write_b64 v184, v[188:189]
	ds_write_b64 v184, v[186:187] offset:33024
	s_waitcnt lgkmcnt(2)
	v_add_f32_e32 v183, v183, v190
	ds_bpermute_b32 v185, v230, v183
	v_pk_mul_f32 v[180:181], v[180:181], v[182:183] op_sel_hi:[1,0]
	v_pk_mul_f32 v[178:179], v[178:179], v[182:183] op_sel_hi:[1,0]
	s_waitcnt vmcnt(19)
	v_pk_fma_f32 v[180:181], v[28:29], v[180:181], v[32:33]
	v_pk_fma_f32 v[178:179], v[26:27], v[178:179], v[30:31]
	s_waitcnt lgkmcnt(0)
	v_add_f32_e32 v182, v183, v185
	ds_bpermute_b32 v183, v231, v182
	s_waitcnt vmcnt(3)
	v_pk_fma_f32 v[180:181], v[156:157], v[180:181], v[160:161]
	v_pk_fma_f32 v[178:179], v[154:155], v[178:179], v[158:159]
	s_waitcnt lgkmcnt(0)
	v_add_f32_e32 v191, v182, v183
	v_fmamk_f32 v175, v191, 0xba800000, v175
	v_fmamk_f32 v174, v191, 0xba800000, v174
	v_fmamk_f32 v177, v191, 0xba800000, v177
	v_fmac_f32_e32 v176, 0xba800000, v191
	v_pk_mul_f32 v[182:183], v[176:177], v[176:177]
	v_pk_mul_f32 v[184:185], v[174:175], v[174:175]
	v_fmamk_f32 v171, v191, 0xba800000, v171
	v_pk_mov_b32 v[186:187], v[184:185], v[182:183] op_sel:[1,0]
	v_mov_b32_e32 v185, v183
	v_pk_add_f32 v[182:183], v[186:187], v[184:185]
	v_fmamk_f32 v170, v191, 0xba800000, v170
	v_fmamk_f32 v173, v191, 0xba800000, v173
	v_fmac_f32_e32 v172, 0xba800000, v191
	v_pk_add_f32 v[182:183], v[182:183], v[182:183] op_sel_hi:[0,1]
	v_pk_mul_f32 v[184:185], v[172:173], v[172:173]
	v_pk_mul_f32 v[186:187], v[170:171], v[170:171]
	v_fmamk_f32 v166, v191, 0xba800000, v166
	v_pk_mov_b32 v[188:189], v[186:187], v[184:185] op_sel:[1,0]
	v_mov_b32_e32 v187, v185
	v_fmamk_f32 v167, v191, 0xba800000, v167
	v_fmac_f32_e32 v168, 0xba800000, v191
	v_mul_f32_e32 v182, v166, v166
	v_pk_add_f32 v[184:185], v[188:189], v[186:187]
	v_fmamk_f32 v169, v191, 0xba800000, v169
	v_pk_fma_f32 v[186:187], v[166:167], v[166:167], v[182:183] op_sel_hi:[1,1,0]
	v_mul_f32_e32 v182, v168, v168
	v_pk_add_f32 v[184:185], v[184:185], v[184:185] op_sel_hi:[0,1]
	v_pk_fma_f32 v[188:189], v[168:169], v[168:169], v[182:183] op_sel_hi:[1,1,0]
	v_fmamk_f32 v165, v191, 0xba800000, v165
	v_fmamk_f32 v164, v191, 0xba800000, v164
	v_fmamk_f32 v163, v191, 0xba800000, v163
	v_fmac_f32_e32 v162, 0xba800000, v191
	v_mul_f32_e32 v186, v162, v162
	v_mul_f32_e32 v188, v163, v163
	v_mul_f32_e32 v182, v164, v164
	v_mul_f32_e32 v184, v165, v165
	v_pk_add_f32 v[186:187], v[186:187], v[188:189]
	v_pk_add_f32 v[182:183], v[182:183], v[184:185]
	v_cvt_pk_bf16_f32 v189, v181, 0
	v_pk_add_f32 v[182:183], v[186:187], v[182:183]
	v_cvt_pk_bf16_f32 v185, v179, 0
	v_add_f32_e32 v182, v182, v183
	ds_bpermute_b32 v183, v226, v182
	v_lshlrev_b32_e32 v189, 16, v189
	v_cvt_pk_bf16_f32 v190, v178, 0
	v_lshlrev_b32_e32 v185, 16, v185
	v_sub_f32_e32 v186, v179, v185
	s_waitcnt lgkmcnt(0)
	v_add_f32_e32 v182, v182, v183
	ds_bpermute_b32 v183, v227, v182
	v_lshlrev_b32_e32 v184, 16, v190
	v_cvt_pk_bf16_f32 v187, v180, 0
	v_lshlrev_b32_e32 v188, 16, v187
	v_sub_f32_e32 v188, v180, v188
	s_waitcnt lgkmcnt(0)
	v_add_f32_e32 v182, v182, v183
	ds_bpermute_b32 v183, v228, v182
	v_sub_f32_e32 v184, v178, v184
	v_cvt_pk_bf16_f32 v186, v186, 0
	v_cvt_pk_bf16_f32 v184, v184, 0
	v_lshlrev_b32_e32 v186, 16, v186
	s_waitcnt lgkmcnt(0)
	v_add_f32_e32 v183, v182, v183
	ds_bpermute_b32 v191, v229, v183
	v_sub_f32_e32 v182, v181, v189
	v_cvt_pk_bf16_f32 v192, v182, 0
	v_and_or_b32 v182, v190, s35, v185
	v_cvt_pk_bf16_f32 v188, v188, 0
	s_waitcnt lgkmcnt(0)
	v_add_f32_e32 v185, v183, v191
	ds_bpermute_b32 v190, v230, v185
	v_and_or_b32 v183, v187, s35, v189
	v_mov_b32_e32 v187, v1
	v_cvt_pk_fp8_f32 v187, v178, v179
	v_and_or_b32 v178, v184, s35, v186
	s_waitcnt lgkmcnt(0)
	v_add_f32_e32 v185, v185, v190
	ds_bpermute_b32 v189, v231, v185
	v_cvt_pk_fp8_f32 v187, v180, v181 op_sel:[0,0,1]
	v_lshlrev_b32_e32 v179, 16, v192
	v_and_or_b32 v179, v188, s35, v179
	s_waitcnt lgkmcnt(0)
	v_add_f32_e32 v180, v185, v189
	v_fmamk_f32 v180, v180, 0x3a800000, v211
	v_mul_f32_e32 v181, 0x4f800000, v180
	v_cmp_gt_f32_e32 vcc, s36, v180
	s_nop 1
	v_cndmask_b32_e32 v184, v180, v181, vcc
	v_sqrt_f32_e32 v185, v184
	v_lshl_add_u64 v[180:181], s[12:13], 0, v[200:201]
	global_store_dword v[180:181], v187, off
	v_add_u32_e32 v180, s47, v237
	v_add_u32_e32 v181, -1, v185
	v_fma_f32 v186, -v181, v185, v184
	v_cmp_ge_f32_e64 s[12:13], 0, v186
	v_add_u32_e32 v186, 1, v185
	ds_write_b64 v180, v[182:183]
	ds_write_b64 v180, v[178:179] offset:33024
	v_cndmask_b32_e64 v181, v185, v181, s[12:13]
	v_fma_f32 v185, -v186, v185, v184
	v_cmp_lt_f32_e64 s[12:13], 0, v185
	s_nop 1
	v_cndmask_b32_e64 v181, v181, v186, s[12:13]
	v_mul_f32_e32 v185, 0x37800000, v181
	v_cndmask_b32_e32 v181, v181, v185, vcc
	v_cmp_class_f32_e32 vcc, v184, v212
	s_nop 1
	v_cndmask_b32_e32 v181, v181, v184, vcc
	v_div_scale_f32 v184, s[12:13], v181, v181, 1.0
	v_rcp_f32_e32 v185, v184
	s_add_i32 s12, s34, 1
	s_ashr_i32 s13, s12, 31
	s_lshl_b64 s[12:13], s[12:13], 10
	v_fma_f32 v178, -v184, v185, 1.0
	v_fmac_f32_e32 v185, v178, v185
	v_div_scale_f32 v178, vcc, 1.0, v181, 1.0
	v_mul_f32_e32 v179, v178, v185
	v_fma_f32 v180, -v184, v179, v178
	v_fmac_f32_e32 v179, v180, v185
	v_fma_f32 v178, -v184, v179, v178
	v_div_fmas_f32 v178, v178, v185, v179
	v_div_fixup_f32 v178, v178, v181, 1.0
	v_pk_mul_f32 v[174:175], v[174:175], v[178:179] op_sel_hi:[1,0]
	v_pk_mul_f32 v[176:177], v[176:177], v[178:179] op_sel_hi:[1,0]
	v_pk_fma_f32 v[174:175], v[2:3], v[174:175], v[6:7]
	v_pk_fma_f32 v[176:177], v[4:5], v[176:177], v[8:9]
	v_pk_fma_f32 v[174:175], v[98:99], v[174:175], v[118:119]
	v_pk_fma_f32 v[176:177], v[100:101], v[176:177], v[120:121]
	v_cvt_pk_bf16_f32 v179, v174, 0
	v_lshlrev_b32_e32 v180, 16, v179
	v_sub_f32_e32 v180, v174, v180
	v_cvt_pk_bf16_f32 v182, v180, 0
	v_cvt_pk_bf16_f32 v180, v175, 0
	v_lshlrev_b32_e32 v180, 16, v180
	v_sub_f32_e32 v181, v175, v180
	v_and_or_b32 v180, v179, s35, v180
	v_mov_b32_e32 v179, v1
	v_cvt_pk_fp8_f32 v179, v174, v175
	v_cvt_pk_bf16_f32 v185, v177, 0
	v_cvt_pk_bf16_f32 v183, v181, 0
	v_cvt_pk_bf16_f32 v181, v176, 0
	v_cvt_pk_fp8_f32 v179, v176, v177 op_sel:[0,0,1]
	v_lshlrev_b32_e32 v185, 16, v185
	v_lshlrev_b32_e32 v184, 16, v181
	v_sub_f32_e32 v186, v177, v185
	v_pk_mul_f32 v[170:171], v[170:171], v[178:179] op_sel_hi:[1,0]
	v_sub_f32_e32 v184, v176, v184
	v_cvt_pk_bf16_f32 v186, v186, 0
	v_lshlrev_b32_e32 v174, 16, v183
	v_lshl_add_u64 v[176:177], v[202:203], 0, s[12:13]
	v_pk_fma_f32 v[170:171], v[10:11], v[170:171], v[18:19]
	v_cvt_pk_bf16_f32 v184, v184, 0
	v_and_or_b32 v181, v181, s35, v185
	v_and_or_b32 v174, v182, s35, v174
	v_lshlrev_b32_e32 v175, 16, v186
	global_store_dword v[176:177], v179, off
	v_add_u32_e32 v176, s48, v234
	v_pk_fma_f32 v[170:171], v[138:139], v[170:171], v[142:143]
	v_and_or_b32 v175, v184, s35, v175
	ds_write_b64 v176, v[180:181]
	ds_write_b64 v176, v[174:175] offset:33024
	v_pk_mul_f32 v[172:173], v[172:173], v[178:179] op_sel_hi:[1,0]
	v_cvt_pk_bf16_f32 v174, v170, 0
	v_pk_fma_f32 v[172:173], v[12:13], v[172:173], v[20:21]
	v_lshlrev_b32_e32 v175, 16, v174
	v_pk_fma_f32 v[172:173], v[140:141], v[172:173], v[144:145]
	v_sub_f32_e32 v175, v170, v175
	v_cvt_pk_bf16_f32 v176, v175, 0
	v_cvt_pk_bf16_f32 v175, v171, 0
	v_cvt_pk_bf16_f32 v181, v173, 0
	v_lshlrev_b32_e32 v175, 16, v175
	v_cvt_pk_bf16_f32 v179, v172, 0
	v_lshlrev_b32_e32 v181, 16, v181
	v_sub_f32_e32 v177, v171, v175
	v_lshlrev_b32_e32 v180, 16, v179
	v_and_or_b32 v174, v174, s35, v175
	v_and_or_b32 v175, v179, s35, v181
	v_mov_b32_e32 v179, v1
	v_cvt_pk_fp8_f32 v179, v170, v171
	s_add_u32 s12, s20, s12
	s_addc_u32 s13, s21, s13
	v_sub_f32_e32 v180, v172, v180
	v_cvt_pk_fp8_f32 v179, v172, v173 op_sel:[0,0,1]
	v_sub_f32_e32 v182, v173, v181
	v_lshl_add_u64 v[172:173], s[12:13], 0, v[0:1]
	v_cvt_pk_bf16_f32 v177, v177, 0
	v_pk_mul_f32 v[166:167], v[166:167], v[178:179] op_sel_hi:[1,0]
	global_store_dword v[172:173], v179, off
	v_pk_fma_f32 v[166:167], v[14:15], v[166:167], v[22:23]
	v_pk_mul_f32 v[168:169], v[168:169], v[178:179] op_sel_hi:[1,0]
	v_pk_fma_f32 v[166:167], v[150:151], v[166:167], v[146:147]
	v_mov_b32_e32 v179, v1
	v_cvt_pk_bf16_f32 v182, v182, 0
	v_lshlrev_b32_e32 v177, 16, v177
	v_cvt_pk_fp8_f32 v179, v166, v167
	v_cvt_pk_bf16_f32 v180, v180, 0
	v_and_or_b32 v170, v176, s35, v177
	v_lshlrev_b32_e32 v171, 16, v182
	v_add_u32_e32 v172, s48, v235
	v_and_or_b32 v171, v180, s35, v171
	ds_write_b64 v172, v[174:175]
	ds_write_b64 v172, v[170:171] offset:33024
	v_pk_fma_f32 v[168:169], v[16:17], v[168:169], v[24:25]
	v_cvt_pk_bf16_f32 v170, v166, 0
	v_pk_fma_f32 v[168:169], v[152:153], v[168:169], v[148:149]
	v_lshlrev_b32_e32 v171, 16, v170
	v_sub_f32_e32 v171, v166, v171
	v_cvt_pk_fp8_f32 v179, v168, v169 op_sel:[0,0,1]
	v_cvt_pk_bf16_f32 v172, v171, 0
	v_cvt_pk_bf16_f32 v171, v167, 0
	v_lshlrev_b32_e32 v171, 16, v171
	v_cvt_pk_bf16_f32 v176, v169, 0
	v_sub_f32_e32 v173, v167, v171
	v_cvt_pk_bf16_f32 v174, v168, 0
	v_lshlrev_b32_e32 v176, 16, v176
	v_cvt_pk_bf16_f32 v173, v173, 0
	v_lshlrev_b32_e32 v175, 16, v174
	v_sub_f32_e32 v177, v169, v176
	v_pk_mul_f32 v[162:163], v[162:163], v[178:179] op_sel_hi:[1,0]
	v_sub_f32_e32 v175, v168, v175
	v_cvt_pk_bf16_f32 v177, v177, 0
	v_lshlrev_b32_e32 v166, 16, v173
	v_lshl_add_u64 v[168:169], s[12:13], 0, v[198:199]
	v_pk_fma_f32 v[162:163], v[26:27], v[162:163], v[30:31]
	v_cvt_pk_bf16_f32 v175, v175, 0
	v_and_or_b32 v170, v170, s35, v171
	v_and_or_b32 v171, v174, s35, v176
	v_and_or_b32 v166, v172, s35, v166
	v_lshlrev_b32_e32 v167, 16, v177
	global_store_dword v[168:169], v179, off
	v_add_u32_e32 v168, s48, v236
	v_pk_fma_f32 v[162:163], v[154:155], v[162:163], v[158:159]
	v_mov_b32_e32 v174, v1
	v_and_or_b32 v167, v175, s35, v167
	ds_write_b64 v168, v[170:171]
	ds_write_b64 v168, v[166:167] offset:33024
	v_pk_mul_f32 v[164:165], v[164:165], v[178:179] op_sel_hi:[1,0]
	v_cvt_pk_bf16_f32 v166, v162, 0
	v_cvt_pk_fp8_f32 v174, v162, v163
	v_pk_fma_f32 v[164:165], v[28:29], v[164:165], v[32:33]
	v_lshlrev_b32_e32 v167, 16, v166
	v_pk_fma_f32 v[164:165], v[156:157], v[164:165], v[160:161]
	v_sub_f32_e32 v167, v162, v167
	v_cvt_pk_bf16_f32 v168, v167, 0
	v_cvt_pk_bf16_f32 v167, v163, 0
	v_cvt_pk_bf16_f32 v172, v165, 0
	v_lshlrev_b32_e32 v167, 16, v167
	v_cvt_pk_bf16_f32 v170, v164, 0
	v_lshlrev_b32_e32 v172, 16, v172
	v_cvt_pk_fp8_f32 v174, v164, v165 op_sel:[0,0,1]
	v_sub_f32_e32 v169, v163, v167
	v_lshlrev_b32_e32 v171, 16, v170
	v_sub_f32_e32 v173, v165, v172
	v_cvt_pk_bf16_f32 v169, v169, 0
	v_sub_f32_e32 v171, v164, v171
	v_cvt_pk_bf16_f32 v173, v173, 0
	v_cvt_pk_bf16_f32 v171, v171, 0
	v_lshlrev_b32_e32 v162, 16, v169
	v_lshlrev_b32_e32 v163, 16, v173
	v_lshl_add_u64 v[164:165], s[12:13], 0, v[200:201]
	v_and_or_b32 v166, v166, s35, v167
	v_and_or_b32 v167, v170, s35, v172
	v_and_or_b32 v162, v168, s35, v162
	v_and_or_b32 v163, v171, s35, v163
	global_store_dword v[164:165], v174, off
	v_add_u32_e32 v164, s48, v237
	ds_write_b64 v164, v[166:167]
	ds_write_b64 v164, v[162:163] offset:33024
	s_waitcnt lgkmcnt(0)
	s_barrier
	ds_read_b128 v[162:165], v238
	ds_read_b128 v[166:169], v238 offset:64
	s_waitcnt lgkmcnt(1)
	v_mfma_f32_16x16x32_bf16 v[170:173], v[162:165], v[34:37], 0
	ds_read_b128 v[174:177], v238 offset:33024
	ds_read_b128 v[178:181], v238 offset:33088
	s_mov_b64 s[34:35], -1
	s_mov_b64 s[12:13], -1
	v_mfma_f32_16x16x32_bf16 v[182:185], v[162:165], v[42:45], 0
	s_waitcnt lgkmcnt(1)
	v_mfma_f32_16x16x32_bf16 v[170:173], v[174:177], v[34:37], v[170:173]
	v_mfma_f32_16x16x32_bf16 v[174:177], v[174:177], v[42:45], v[182:185]
	v_mfma_f32_16x16x32_bf16 v[170:173], v[162:165], v[38:41], v[170:173]
	v_mfma_f32_16x16x32_bf16 v[162:165], v[162:165], v[46:49], v[174:177]
	v_mfma_f32_16x16x32_bf16 v[170:173], v[166:169], v[50:53], v[170:173]
	v_mfma_f32_16x16x32_bf16 v[162:165], v[166:169], v[58:61], v[162:165]
	s_waitcnt lgkmcnt(0)
	v_mfma_f32_16x16x32_bf16 v[170:173], v[178:181], v[50:53], v[170:173]
	v_mfma_f32_16x16x32_bf16 v[162:165], v[178:181], v[58:61], v[162:165]
	v_mfma_f32_16x16x32_bf16 v[170:173], v[166:169], v[54:57], v[170:173]
	v_mfma_f32_16x16x32_bf16 v[162:165], v[166:169], v[62:65], v[162:165]
	ds_read_b128 v[166:169], v238 offset:128
	ds_read_b128 v[174:177], v238 offset:192
	ds_read_b128 v[178:181], v238 offset:33152
	ds_read_b128 v[182:185], v238 offset:33216
	s_waitcnt lgkmcnt(3)
	v_mfma_f32_16x16x32_bf16 v[170:173], v[166:169], v[66:69], v[170:173]
	v_mfma_f32_16x16x32_bf16 v[162:165], v[166:169], v[74:77], v[162:165]
	s_waitcnt lgkmcnt(1)
	v_mfma_f32_16x16x32_bf16 v[170:173], v[178:181], v[66:69], v[170:173]
	v_mfma_f32_16x16x32_bf16 v[162:165], v[178:181], v[74:77], v[162:165]
	v_mfma_f32_16x16x32_bf16 v[170:173], v[166:169], v[70:73], v[170:173]
	v_mfma_f32_16x16x32_bf16 v[162:165], v[166:169], v[78:81], v[162:165]
	v_mfma_f32_16x16x32_bf16 v[166:169], v[174:177], v[82:85], v[170:173]
	v_mfma_f32_16x16x32_bf16 v[162:165], v[174:177], v[90:93], v[162:165]
	s_waitcnt lgkmcnt(0)
	v_mfma_f32_16x16x32_bf16 v[166:169], v[182:185], v[82:85], v[166:169]
	v_mfma_f32_16x16x32_bf16 v[162:165], v[182:185], v[90:93], v[162:165]
	v_mfma_f32_16x16x32_bf16 v[166:169], v[174:177], v[86:89], v[166:169]
	v_mfma_f32_16x16x32_bf16 v[162:165], v[174:177], v[94:97], v[162:165]
	s_nop 7
	ds_write2_b32 v239, v166, v162 offset1:16
	ds_write2_b32 v239, v167, v163 offset0:32 offset1:48
	ds_write2_b32 v239, v168, v164 offset0:64 offset1:80
	ds_write2_b32 v239, v169, v165 offset0:96 offset1:112
	s_waitcnt lgkmcnt(0)
	s_barrier
	ds_read2st64_b32 v[162:163], v233 offset1:8
	ds_read2st64_b32 v[164:165], v233 offset0:16 offset1:24
	s_waitcnt lgkmcnt(1)
	v_add_f32_e32 v162, v242, v162
	ds_read2st64_b32 v[166:167], v233 offset0:32 offset1:40
	v_add_f32_e32 v168, v162, v163
	ds_read2st64_b32 v[162:163], v233 offset0:48 offset1:56
	s_waitcnt lgkmcnt(2)
	v_add_f32_e32 v164, v168, v164
	v_add_f32_e32 v164, v164, v165
	s_waitcnt lgkmcnt(1)
	v_add_f32_e32 v164, v164, v166
	v_add_f32_e32 v164, v164, v167
	s_waitcnt lgkmcnt(0)
	v_add_f32_e32 v162, v164, v162
	v_add_f32_e32 v165, v162, v163
	ds_bpermute_b32 v162, v230, v165
	ds_bpermute_b32 v163, v230, v232
	s_waitcnt lgkmcnt(1)
	v_cmp_nlt_f32_e32 vcc, v165, v162
	s_and_saveexec_b64 s[36:37], vcc
	s_cbranch_execz .LBB0_988
	v_cmp_eq_f32_e32 vcc, v165, v162
	s_waitcnt lgkmcnt(0)
	v_cmp_lt_i32_e64 s[12:13], v163, v232
	s_and_b64 s[12:13], vcc, s[12:13]
	s_orn2_b64 s[12:13], s[12:13], exec
